# speedup vs baseline: 1.0012x; 1.0012x over previous
.Lp_next:
	s_mov_b64 exec, 1
	ds_add_rtn_u32 v10, v59, v60
	s_mov_b64 exec, -1
	s_waitcnt lgkmcnt(0)
	v_readfirstlane_b32 s34, v10
	s_cmp_lt_u32 s34, s62
	s_cselect_b32 s45, s64, s65
	s_cselect_b32 s46, 0, s62
	s_cselect_b32 s48, s62, s63
	s_sub_u32 s47, s34, s46
	s_cmp_ge_u32 s47, s48
	s_cbranch_scc1 .Lp_done
	s_lshl_b32 s47, s47, 3
	s_add_u32 s45, s45, s47
	v_mov_b32_e32 v11, s45
	ds_read2_b32 v[12:13], v11 offset1:1
	s_waitcnt lgkmcnt(0)
	v_readfirstlane_b32 s35, v12
	v_readfirstlane_b32 s36, v13
	s_nop 1
	v_mov_b32_e32 v10, s35
	v_mov_b32_e32 v11, s36
	v_cndmask_b32_e64 v12, v10, v11, s[54:55]
	v_cndmask_b32_e64 v13, v10, v11, s[56:57]
	v_lshl_add_u32 v12, v12, 3, v61
	v_lshl_add_u32 v14, v13, 4, v62
	ds_read_b64 v[2:3], v12
	ds_read_b128 v[4:7], v14
	v_mad_u32_u24 v9, v13, s49, v58
	v_mov_b32_e32 v8, v56
	s_waitcnt lgkmcnt(0)
	v_add_u32_e32 v2, v2, v55
	v_and_b32_e32 v3, v3, v63
	s_nop 0
	v_readlane_b32 s41, v3, 0
	v_readlane_b32 s42, v3, 4
	s_max_u32 s43, s41, s42
	s_cmp_eq_u32 s43, 0
	s_cbranch_scc1 .Lp_zero
	ds_read_b64 v[36:37], v2
	v_cmp_gt_u32_e32 vcc, v3, v8
	v_add_u32_e32 v2, 64, v2
	v_add_u32_e32 v8, 16, v8
	v_mov_b32_e32 v33, 0x3c00
	s_waitcnt lgkmcnt(0)
	v_perm_b32 v32, v37, v36, v57
	v_cndmask_b32_e32 v33, 0, v33, vcc
	s_nop 0
	v_cndmask_b32_e32 v32, 0, v32, vcc
	s_nop 1
	v_mfma_f32_32x32x16_f16 v[96:111], v[32:35], v[64:67], 0
	v_mfma_f32_32x32x16_f16 v[112:127], v[32:35], v[68:71], 0
	s_nop 10
	s_mov_b32 s45, s43
	s_min_u32 s46, s45, 16
	s_cmp_eq_u32 s46, 16
	s_cbranch_scc1 .Lf16
	s_cmp_eq_u32 s46, 15
	s_cbranch_scc1 .Lf15
	s_cmp_eq_u32 s46, 14
	s_cbranch_scc1 .Lf14
	s_cmp_eq_u32 s46, 13
	s_cbranch_scc1 .Lf13
	s_cmp_eq_u32 s46, 12
	s_cbranch_scc1 .Lf12
	s_cmp_eq_u32 s46, 11
	s_cbranch_scc1 .Lf11
	s_cmp_eq_u32 s46, 10
	s_cbranch_scc1 .Lf10
	s_cmp_eq_u32 s46, 9
	s_cbranch_scc1 .Lf9
	s_cmp_eq_u32 s46, 8
	s_cbranch_scc1 .Lf8
	s_cmp_eq_u32 s46, 7
	s_cbranch_scc1 .Lf7
	s_cmp_eq_u32 s46, 6
	s_cbranch_scc1 .Lf6
	s_cmp_eq_u32 s46, 5
	s_cbranch_scc1 .Lf5
	s_cmp_eq_u32 s46, 4
	s_cbranch_scc1 .Lf4
	s_cmp_eq_u32 s46, 3
	s_cbranch_scc1 .Lf3
	s_cmp_eq_u32 s46, 2
	s_cbranch_scc1 .Lf2
.Lf1:
	v_add_f32_e64 v24, |v96|, 0
	s_nop 10
	v_mfma_f32_32x32x16_f16 v[96:111], v[32:35], v[72:75], 0
	v_add_f32_e64 v25, |v112|, 0
	s_nop 10
	v_mfma_f32_32x32x16_f16 v[112:127], v[32:35], v[76:79], 0
	v_add_f32_e64 v26, |v96|, 0
	s_nop 10
	v_mfma_f32_32x32x16_f16 v[96:111], v[32:35], v[80:83], 0
	v_add_f32_e64 v27, |v112|, 0
	s_nop 10
	v_mfma_f32_32x32x16_f16 v[112:127], v[32:35], v[84:87], 0
	v_add_f32_e64 v28, |v96|, 0
	s_nop 10
	v_mfma_f32_32x32x16_f16 v[96:111], v[32:35], v[88:91], 0
	v_add_f32_e64 v29, |v112|, 0
	s_nop 10
	v_mfma_f32_32x32x16_f16 v[112:127], v[32:35], v[92:95], 0
	v_add_f32_e64 v30, |v96|, 0
	s_nop 10
	v_add_f32_e64 v31, |v112|, 0
	s_nop 10
	s_branch .Lafter_first
.Lf2:
	v_add_f32_e64 v24, |v96|, |v97|
	s_nop 10
	v_mfma_f32_32x32x16_f16 v[96:111], v[32:35], v[72:75], 0
	v_add_f32_e64 v25, |v112|, |v113|
	s_nop 10
	v_mfma_f32_32x32x16_f16 v[112:127], v[32:35], v[76:79], 0
	v_add_f32_e64 v26, |v96|, |v97|
	s_nop 10
	v_mfma_f32_32x32x16_f16 v[96:111], v[32:35], v[80:83], 0
	v_add_f32_e64 v27, |v112|, |v113|
	s_nop 10
	v_mfma_f32_32x32x16_f16 v[112:127], v[32:35], v[84:87], 0
	v_add_f32_e64 v28, |v96|, |v97|
	s_nop 10
	v_mfma_f32_32x32x16_f16 v[96:111], v[32:35], v[88:91], 0
	v_add_f32_e64 v29, |v112|, |v113|
	s_nop 10
	v_mfma_f32_32x32x16_f16 v[112:127], v[32:35], v[92:95], 0
	v_add_f32_e64 v30, |v96|, |v97|
	s_nop 10
	v_add_f32_e64 v31, |v112|, |v113|
	s_nop 10
	s_branch .Lafter_first
.Lf3:
	v_add_f32_e64 v38, |v96|, |v97|
	v_add_f32_e64 v24, v38, |v98|
	s_nop 9
	v_mfma_f32_32x32x16_f16 v[96:111], v[32:35], v[72:75], 0
	v_add_f32_e64 v38, |v112|, |v113|
	v_add_f32_e64 v25, v38, |v114|
	s_nop 9
	v_mfma_f32_32x32x16_f16 v[112:127], v[32:35], v[76:79], 0
	v_add_f32_e64 v38, |v96|, |v97|
	v_add_f32_e64 v26, v38, |v98|
	s_nop 9
	v_mfma_f32_32x32x16_f16 v[96:111], v[32:35], v[80:83], 0
	v_add_f32_e64 v38, |v112|, |v113|
	v_add_f32_e64 v27, v38, |v114|
	s_nop 9
	v_mfma_f32_32x32x16_f16 v[112:127], v[32:35], v[84:87], 0
	v_add_f32_e64 v38, |v96|, |v97|
	v_add_f32_e64 v28, v38, |v98|
	s_nop 9
	v_mfma_f32_32x32x16_f16 v[96:111], v[32:35], v[88:91], 0
	v_add_f32_e64 v38, |v112|, |v113|
	v_add_f32_e64 v29, v38, |v114|
	s_nop 9
	v_mfma_f32_32x32x16_f16 v[112:127], v[32:35], v[92:95], 0
	v_add_f32_e64 v38, |v96|, |v97|
	v_add_f32_e64 v30, v38, |v98|
	s_nop 9
	v_add_f32_e64 v38, |v112|, |v113|
	v_add_f32_e64 v31, v38, |v114|
	s_nop 9
	s_branch .Lafter_first

.Lf5:
	v_add_f32_e64 v38, |v96|, |v97|
	v_add_f32_e64 v39, |v98|, |v99|
	v_add_f32_e64 v38, v38, |v100|
	v_add_f32_e32 v24, v38, v39
	s_nop 7
	v_mfma_f32_32x32x16_f16 v[96:111], v[32:35], v[72:75], 0
	v_add_f32_e64 v38, |v112|, |v113|
	v_add_f32_e64 v39, |v114|, |v115|
	v_add_f32_e64 v38, v38, |v116|
	v_add_f32_e32 v25, v38, v39
	s_nop 7
	v_mfma_f32_32x32x16_f16 v[112:127], v[32:35], v[76:79], 0
	v_add_f32_e64 v38, |v96|, |v97|
	v_add_f32_e64 v39, |v98|, |v99|
	v_add_f32_e64 v38, v38, |v100|
	v_add_f32_e32 v26, v38, v39
	s_nop 7
	v_mfma_f32_32x32x16_f16 v[96:111], v[32:35], v[80:83], 0
	v_add_f32_e64 v38, |v112|, |v113|
	v_add_f32_e64 v39, |v114|, |v115|
	v_add_f32_e64 v38, v38, |v116|
	v_add_f32_e32 v27, v38, v39
	s_nop 7
	v_mfma_f32_32x32x16_f16 v[112:127], v[32:35], v[84:87], 0
	v_add_f32_e64 v38, |v96|, |v97|
	v_add_f32_e64 v39, |v98|, |v99|
	v_add_f32_e64 v38, v38, |v100|
	v_add_f32_e32 v28, v38, v39
	s_nop 7
	v_mfma_f32_32x32x16_f16 v[96:111], v[32:35], v[88:91], 0
	v_add_f32_e64 v38, |v112|, |v113|
	v_add_f32_e64 v39, |v114|, |v115|
	v_add_f32_e64 v38, v38, |v116|
	v_add_f32_e32 v29, v38, v39
	s_nop 7
	v_mfma_f32_32x32x16_f16 v[112:127], v[32:35], v[92:95], 0
	v_add_f32_e64 v38, |v96|, |v97|
	v_add_f32_e64 v39, |v98|, |v99|
	v_add_f32_e64 v38, v38, |v100|
	v_add_f32_e32 v30, v38, v39
	s_nop 7
	v_add_f32_e64 v38, |v112|, |v113|
	v_add_f32_e64 v39, |v114|, |v115|
	v_add_f32_e64 v38, v38, |v116|
	v_add_f32_e32 v31, v38, v39
	s_nop 7
	s_branch .Lafter_first
.Lf6:
	v_add_f32_e64 v38, |v96|, |v97|
	v_add_f32_e64 v39, |v98|, |v99|
	v_add_f32_e64 v38, v38, |v100|
	v_add_f32_e64 v39, v39, |v101|
	v_add_f32_e32 v24, v38, v39
	s_nop 6
	v_mfma_f32_32x32x16_f16 v[96:111], v[32:35], v[72:75], 0
	v_add_f32_e64 v38, |v112|, |v113|
	v_add_f32_e64 v39, |v114|, |v115|
	v_add_f32_e64 v38, v38, |v116|
	v_add_f32_e64 v39, v39, |v117|
	v_add_f32_e32 v25, v38, v39
	s_nop 6
	v_mfma_f32_32x32x16_f16 v[112:127], v[32:35], v[76:79], 0
	v_add_f32_e64 v38, |v96|, |v97|
	v_add_f32_e64 v39, |v98|, |v99|
	v_add_f32_e64 v38, v38, |v100|
	v_add_f32_e64 v39, v39, |v101|
	v_add_f32_e32 v26, v38, v39
	s_nop 6
	v_mfma_f32_32x32x16_f16 v[96:111], v[32:35], v[80:83], 0
	v_add_f32_e64 v38, |v112|, |v113|
	v_add_f32_e64 v39, |v114|, |v115|
	v_add_f32_e64 v38, v38, |v116|
	v_add_f32_e64 v39, v39, |v117|
	v_add_f32_e32 v27, v38, v39
	s_nop 6
	v_mfma_f32_32x32x16_f16 v[112:127], v[32:35], v[84:87], 0
	v_add_f32_e64 v38, |v96|, |v97|
	v_add_f32_e64 v39, |v98|, |v99|
	v_add_f32_e64 v38, v38, |v100|
	v_add_f32_e64 v39, v39, |v101|
	v_add_f32_e32 v28, v38, v39
	s_nop 6
	v_mfma_f32_32x32x16_f16 v[96:111], v[32:35], v[88:91], 0
	v_add_f32_e64 v38, |v112|, |v113|
	v_add_f32_e64 v39, |v114|, |v115|
	v_add_f32_e64 v38, v38, |v116|
	v_add_f32_e64 v39, v39, |v117|
	v_add_f32_e32 v29, v38, v39
	s_nop 6
	v_mfma_f32_32x32x16_f16 v[112:127], v[32:35], v[92:95], 0
	v_add_f32_e64 v38, |v96|, |v97|
	v_add_f32_e64 v39, |v98|, |v99|
	v_add_f32_e64 v38, v38, |v100|
	v_add_f32_e64 v39, v39, |v101|
	v_add_f32_e32 v30, v38, v39
	s_nop 6
	v_add_f32_e64 v38, |v112|, |v113|
	v_add_f32_e64 v39, |v114|, |v115|
	v_add_f32_e64 v38, v38, |v116|
	v_add_f32_e64 v39, v39, |v117|
	v_add_f32_e32 v31, v38, v39
	s_nop 6
	s_branch .Lafter_first
.Lf7:
	v_add_f32_e64 v38, |v96|, |v97|
	v_add_f32_e64 v39, |v98|, |v99|
	v_add_f32_e64 v38, v38, |v100|
	v_add_f32_e64 v39, v39, |v101|
	v_add_f32_e64 v38, v38, |v102|
	v_add_f32_e32 v24, v38, v39
	s_nop 5
	v_mfma_f32_32x32x16_f16 v[96:111], v[32:35], v[72:75], 0
	v_add_f32_e64 v38, |v112|, |v113|
	v_add_f32_e64 v39, |v114|, |v115|
	v_add_f32_e64 v38, v38, |v116|
	v_add_f32_e64 v39, v39, |v117|
	v_add_f32_e64 v38, v38, |v118|
	v_add_f32_e32 v25, v38, v39
	s_nop 5
	v_mfma_f32_32x32x16_f16 v[112:127], v[32:35], v[76:79], 0
	v_add_f32_e64 v38, |v96|, |v97|
	v_add_f32_e64 v39, |v98|, |v99|
	v_add_f32_e64 v38, v38, |v100|
	v_add_f32_e64 v39, v39, |v101|
	v_add_f32_e64 v38, v38, |v102|
	v_add_f32_e32 v26, v38, v39
	s_nop 5
	v_mfma_f32_32x32x16_f16 v[96:111], v[32:35], v[80:83], 0
	v_add_f32_e64 v38, |v112|, |v113|
	v_add_f32_e64 v39, |v114|, |v115|
	v_add_f32_e64 v38, v38, |v116|
	v_add_f32_e64 v39, v39, |v117|
	v_add_f32_e64 v38, v38, |v118|
	v_add_f32_e32 v27, v38, v39
	s_nop 5
	v_mfma_f32_32x32x16_f16 v[112:127], v[32:35], v[84:87], 0
	v_add_f32_e64 v38, |v96|, |v97|
	v_add_f32_e64 v39, |v98|, |v99|
	v_add_f32_e64 v38, v38, |v100|
	v_add_f32_e64 v39, v39, |v101|
	v_add_f32_e64 v38, v38, |v102|
	v_add_f32_e32 v28, v38, v39
	s_nop 5
	v_mfma_f32_32x32x16_f16 v[96:111], v[32:35], v[88:91], 0
	v_add_f32_e64 v38, |v112|, |v113|
	v_add_f32_e64 v39, |v114|, |v115|
	v_add_f32_e64 v38, v38, |v116|
	v_add_f32_e64 v39, v39, |v117|
	v_add_f32_e64 v38, v38, |v118|
	v_add_f32_e32 v29, v38, v39
	s_nop 5
	v_mfma_f32_32x32x16_f16 v[112:127], v[32:35], v[92:95], 0
	v_add_f32_e64 v38, |v96|, |v97|
	v_add_f32_e64 v39, |v98|, |v99|
	v_add_f32_e64 v38, v38, |v100|
	v_add_f32_e64 v39, v39, |v101|
	v_add_f32_e64 v38, v38, |v102|
	v_add_f32_e32 v30, v38, v39
	s_nop 5
	v_add_f32_e64 v38, |v112|, |v113|
	v_add_f32_e64 v39, |v114|, |v115|
	v_add_f32_e64 v38, v38, |v116|
	v_add_f32_e64 v39, v39, |v117|
	v_add_f32_e64 v38, v38, |v118|
	v_add_f32_e32 v31, v38, v39
	s_nop 5
	s_branch .Lafter_first

.Lf9:
	v_add_f32_e64 v38, |v96|, |v97|
	v_add_f32_e64 v39, |v98|, |v99|
	v_add_f32_e64 v38, v38, |v100|
	v_add_f32_e64 v39, v39, |v101|
	v_add_f32_e64 v38, v38, |v102|
	v_add_f32_e64 v39, v39, |v103|
	v_add_f32_e64 v38, v38, |v104|
	v_add_f32_e32 v24, v38, v39
	s_nop 3
	v_mfma_f32_32x32x16_f16 v[96:111], v[32:35], v[72:75], 0
	v_add_f32_e64 v38, |v112|, |v113|
	v_add_f32_e64 v39, |v114|, |v115|
	v_add_f32_e64 v38, v38, |v116|
	v_add_f32_e64 v39, v39, |v117|
	v_add_f32_e64 v38, v38, |v118|
	v_add_f32_e64 v39, v39, |v119|
	v_add_f32_e64 v38, v38, |v120|
	v_add_f32_e32 v25, v38, v39
	s_nop 3
	v_mfma_f32_32x32x16_f16 v[112:127], v[32:35], v[76:79], 0
	v_add_f32_e64 v38, |v96|, |v97|
	v_add_f32_e64 v39, |v98|, |v99|
	v_add_f32_e64 v38, v38, |v100|
	v_add_f32_e64 v39, v39, |v101|
	v_add_f32_e64 v38, v38, |v102|
	v_add_f32_e64 v39, v39, |v103|
	v_add_f32_e64 v38, v38, |v104|
	v_add_f32_e32 v26, v38, v39
	s_nop 3
	v_mfma_f32_32x32x16_f16 v[96:111], v[32:35], v[80:83], 0
	v_add_f32_e64 v38, |v112|, |v113|
	v_add_f32_e64 v39, |v114|, |v115|
	v_add_f32_e64 v38, v38, |v116|
	v_add_f32_e64 v39, v39, |v117|
	v_add_f32_e64 v38, v38, |v118|
	v_add_f32_e64 v39, v39, |v119|
	v_add_f32_e64 v38, v38, |v120|
	v_add_f32_e32 v27, v38, v39
	s_nop 3
	v_mfma_f32_32x32x16_f16 v[112:127], v[32:35], v[84:87], 0
	v_add_f32_e64 v38, |v96|, |v97|
	v_add_f32_e64 v39, |v98|, |v99|
	v_add_f32_e64 v38, v38, |v100|
	v_add_f32_e64 v39, v39, |v101|
	v_add_f32_e64 v38, v38, |v102|
	v_add_f32_e64 v39, v39, |v103|
	v_add_f32_e64 v38, v38, |v104|
	v_add_f32_e32 v28, v38, v39
	s_nop 3
	v_mfma_f32_32x32x16_f16 v[96:111], v[32:35], v[88:91], 0
	v_add_f32_e64 v38, |v112|, |v113|
	v_add_f32_e64 v39, |v114|, |v115|
	v_add_f32_e64 v38, v38, |v116|
	v_add_f32_e64 v39, v39, |v117|
	v_add_f32_e64 v38, v38, |v118|
	v_add_f32_e64 v39, v39, |v119|
	v_add_f32_e64 v38, v38, |v120|
	v_add_f32_e32 v29, v38, v39
	s_nop 3
	v_mfma_f32_32x32x16_f16 v[112:127], v[32:35], v[92:95], 0
	v_add_f32_e64 v38, |v96|, |v97|
	v_add_f32_e64 v39, |v98|, |v99|
	v_add_f32_e64 v38, v38, |v100|
	v_add_f32_e64 v39, v39, |v101|
	v_add_f32_e64 v38, v38, |v102|
	v_add_f32_e64 v39, v39, |v103|
	v_add_f32_e64 v38, v38, |v104|
	v_add_f32_e32 v30, v38, v39
	s_nop 3
	v_add_f32_e64 v38, |v112|, |v113|
	v_add_f32_e64 v39, |v114|, |v115|
	v_add_f32_e64 v38, v38, |v116|
	v_add_f32_e64 v39, v39, |v117|
	v_add_f32_e64 v38, v38, |v118|
	v_add_f32_e64 v39, v39, |v119|
	v_add_f32_e64 v38, v38, |v120|
	v_add_f32_e32 v31, v38, v39
	s_nop 3
	s_branch .Lafter_first
.Lf10:
	v_add_f32_e64 v38, |v96|, |v97|
	v_add_f32_e64 v39, |v98|, |v99|
	v_add_f32_e64 v38, v38, |v100|
	v_add_f32_e64 v39, v39, |v101|
	v_add_f32_e64 v38, v38, |v102|
	v_add_f32_e64 v39, v39, |v103|
	v_add_f32_e64 v38, v38, |v104|
	v_add_f32_e64 v39, v39, |v105|
	v_add_f32_e32 v24, v38, v39
	s_nop 2
	v_mfma_f32_32x32x16_f16 v[96:111], v[32:35], v[72:75], 0
	v_add_f32_e64 v38, |v112|, |v113|
	v_add_f32_e64 v39, |v114|, |v115|
	v_add_f32_e64 v38, v38, |v116|
	v_add_f32_e64 v39, v39, |v117|
	v_add_f32_e64 v38, v38, |v118|
	v_add_f32_e64 v39, v39, |v119|
	v_add_f32_e64 v38, v38, |v120|
	v_add_f32_e64 v39, v39, |v121|
	v_add_f32_e32 v25, v38, v39
	s_nop 2
	v_mfma_f32_32x32x16_f16 v[112:127], v[32:35], v[76:79], 0
	v_add_f32_e64 v38, |v96|, |v97|
	v_add_f32_e64 v39, |v98|, |v99|
	v_add_f32_e64 v38, v38, |v100|
	v_add_f32_e64 v39, v39, |v101|
	v_add_f32_e64 v38, v38, |v102|
	v_add_f32_e64 v39, v39, |v103|
	v_add_f32_e64 v38, v38, |v104|
	v_add_f32_e64 v39, v39, |v105|
	v_add_f32_e32 v26, v38, v39
	s_nop 2
	v_mfma_f32_32x32x16_f16 v[96:111], v[32:35], v[80:83], 0
	v_add_f32_e64 v38, |v112|, |v113|
	v_add_f32_e64 v39, |v114|, |v115|
	v_add_f32_e64 v38, v38, |v116|
	v_add_f32_e64 v39, v39, |v117|
	v_add_f32_e64 v38, v38, |v118|
	v_add_f32_e64 v39, v39, |v119|
	v_add_f32_e64 v38, v38, |v120|
	v_add_f32_e64 v39, v39, |v121|
	v_add_f32_e32 v27, v38, v39
	s_nop 2
	v_mfma_f32_32x32x16_f16 v[112:127], v[32:35], v[84:87], 0
	v_add_f32_e64 v38, |v96|, |v97|
	v_add_f32_e64 v39, |v98|, |v99|
	v_add_f32_e64 v38, v38, |v100|
	v_add_f32_e64 v39, v39, |v101|
	v_add_f32_e64 v38, v38, |v102|
	v_add_f32_e64 v39, v39, |v103|
	v_add_f32_e64 v38, v38, |v104|
	v_add_f32_e64 v39, v39, |v105|
	v_add_f32_e32 v28, v38, v39
	s_nop 2
	v_mfma_f32_32x32x16_f16 v[96:111], v[32:35], v[88:91], 0
	v_add_f32_e64 v38, |v112|, |v113|
	v_add_f32_e64 v39, |v114|, |v115|
	v_add_f32_e64 v38, v38, |v116|
	v_add_f32_e64 v39, v39, |v117|
	v_add_f32_e64 v38, v38, |v118|
	v_add_f32_e64 v39, v39, |v119|
	v_add_f32_e64 v38, v38, |v120|
	v_add_f32_e64 v39, v39, |v121|
	v_add_f32_e32 v29, v38, v39
	s_nop 2
	v_mfma_f32_32x32x16_f16 v[112:127], v[32:35], v[92:95], 0
	v_add_f32_e64 v38, |v96|, |v97|
	v_add_f32_e64 v39, |v98|, |v99|
	v_add_f32_e64 v38, v38, |v100|
	v_add_f32_e64 v39, v39, |v101|
	v_add_f32_e64 v38, v38, |v102|
	v_add_f32_e64 v39, v39, |v103|
	v_add_f32_e64 v38, v38, |v104|
	v_add_f32_e64 v39, v39, |v105|
	v_add_f32_e32 v30, v38, v39
	s_nop 2
	v_add_f32_e64 v38, |v112|, |v113|
	v_add_f32_e64 v39, |v114|, |v115|
	v_add_f32_e64 v38, v38, |v116|
	v_add_f32_e64 v39, v39, |v117|
	v_add_f32_e64 v38, v38, |v118|
	v_add_f32_e64 v39, v39, |v119|
	v_add_f32_e64 v38, v38, |v120|
	v_add_f32_e64 v39, v39, |v121|
	v_add_f32_e32 v31, v38, v39
	s_nop 2
	s_branch .Lafter_first
.Lf11:
	v_add_f32_e64 v38, |v96|, |v97|
	v_add_f32_e64 v39, |v98|, |v99|
	v_add_f32_e64 v38, v38, |v100|
	v_add_f32_e64 v39, v39, |v101|
	v_add_f32_e64 v38, v38, |v102|
	v_add_f32_e64 v39, v39, |v103|
	v_add_f32_e64 v38, v38, |v104|
	v_add_f32_e64 v39, v39, |v105|
	v_add_f32_e64 v38, v38, |v106|
	v_add_f32_e32 v24, v38, v39
	s_nop 1
	v_mfma_f32_32x32x16_f16 v[96:111], v[32:35], v[72:75], 0
	v_add_f32_e64 v38, |v112|, |v113|
	v_add_f32_e64 v39, |v114|, |v115|
	v_add_f32_e64 v38, v38, |v116|
	v_add_f32_e64 v39, v39, |v117|
	v_add_f32_e64 v38, v38, |v118|
	v_add_f32_e64 v39, v39, |v119|
	v_add_f32_e64 v38, v38, |v120|
	v_add_f32_e64 v39, v39, |v121|
	v_add_f32_e64 v38, v38, |v122|
	v_add_f32_e32 v25, v38, v39
	s_nop 1
	v_mfma_f32_32x32x16_f16 v[112:127], v[32:35], v[76:79], 0
	v_add_f32_e64 v38, |v96|, |v97|
	v_add_f32_e64 v39, |v98|, |v99|
	v_add_f32_e64 v38, v38, |v100|
	v_add_f32_e64 v39, v39, |v101|
	v_add_f32_e64 v38, v38, |v102|
	v_add_f32_e64 v39, v39, |v103|
	v_add_f32_e64 v38, v38, |v104|
	v_add_f32_e64 v39, v39, |v105|
	v_add_f32_e64 v38, v38, |v106|
	v_add_f32_e32 v26, v38, v39
	s_nop 1
	v_mfma_f32_32x32x16_f16 v[96:111], v[32:35], v[80:83], 0
	v_add_f32_e64 v38, |v112|, |v113|
	v_add_f32_e64 v39, |v114|, |v115|
	v_add_f32_e64 v38, v38, |v116|
	v_add_f32_e64 v39, v39, |v117|
	v_add_f32_e64 v38, v38, |v118|
	v_add_f32_e64 v39, v39, |v119|
	v_add_f32_e64 v38, v38, |v120|
	v_add_f32_e64 v39, v39, |v121|
	v_add_f32_e64 v38, v38, |v122|
	v_add_f32_e32 v27, v38, v39
	s_nop 1
	v_mfma_f32_32x32x16_f16 v[112:127], v[32:35], v[84:87], 0
	v_add_f32_e64 v38, |v96|, |v97|
	v_add_f32_e64 v39, |v98|, |v99|
	v_add_f32_e64 v38, v38, |v100|
	v_add_f32_e64 v39, v39, |v101|
	v_add_f32_e64 v38, v38, |v102|
	v_add_f32_e64 v39, v39, |v103|
	v_add_f32_e64 v38, v38, |v104|
	v_add_f32_e64 v39, v39, |v105|
	v_add_f32_e64 v38, v38, |v106|
	v_add_f32_e32 v28, v38, v39
	s_nop 1
	v_mfma_f32_32x32x16_f16 v[96:111], v[32:35], v[88:91], 0
	v_add_f32_e64 v38, |v112|, |v113|
	v_add_f32_e64 v39, |v114|, |v115|
	v_add_f32_e64 v38, v38, |v116|
	v_add_f32_e64 v39, v39, |v117|
	v_add_f32_e64 v38, v38, |v118|
	v_add_f32_e64 v39, v39, |v119|
	v_add_f32_e64 v38, v38, |v120|
	v_add_f32_e64 v39, v39, |v121|
	v_add_f32_e64 v38, v38, |v122|
	v_add_f32_e32 v29, v38, v39
	s_nop 1
	v_mfma_f32_32x32x16_f16 v[112:127], v[32:35], v[92:95], 0
	v_add_f32_e64 v38, |v96|, |v97|
	v_add_f32_e64 v39, |v98|, |v99|
	v_add_f32_e64 v38, v38, |v100|
	v_add_f32_e64 v39, v39, |v101|
	v_add_f32_e64 v38, v38, |v102|
	v_add_f32_e64 v39, v39, |v103|
	v_add_f32_e64 v38, v38, |v104|
	v_add_f32_e64 v39, v39, |v105|
	v_add_f32_e64 v38, v38, |v106|
	v_add_f32_e32 v30, v38, v39
	s_nop 1
	v_add_f32_e64 v38, |v112|, |v113|
	v_add_f32_e64 v39, |v114|, |v115|
	v_add_f32_e64 v38, v38, |v116|
	v_add_f32_e64 v39, v39, |v117|
	v_add_f32_e64 v38, v38, |v118|
	v_add_f32_e64 v39, v39, |v119|
	v_add_f32_e64 v38, v38, |v120|
	v_add_f32_e64 v39, v39, |v121|
	v_add_f32_e64 v38, v38, |v122|
	v_add_f32_e32 v31, v38, v39
	s_nop 1
	s_branch .Lafter_first

.Lf13:
	v_add_f32_e64 v38, |v96|, |v97|
	v_add_f32_e64 v39, |v98|, |v99|
	v_add_f32_e64 v38, v38, |v100|
	v_add_f32_e64 v39, v39, |v101|
	v_add_f32_e64 v38, v38, |v102|
	v_add_f32_e64 v39, v39, |v103|
	v_add_f32_e64 v38, v38, |v104|
	v_add_f32_e64 v39, v39, |v105|
	v_add_f32_e64 v38, v38, |v106|
	v_add_f32_e64 v39, v39, |v107|
	v_add_f32_e64 v38, v38, |v108|
	v_add_f32_e32 v24, v38, v39
	v_mfma_f32_32x32x16_f16 v[96:111], v[32:35], v[72:75], 0
	v_add_f32_e64 v38, |v112|, |v113|
	v_add_f32_e64 v39, |v114|, |v115|
	v_add_f32_e64 v38, v38, |v116|
	v_add_f32_e64 v39, v39, |v117|
	v_add_f32_e64 v38, v38, |v118|
	v_add_f32_e64 v39, v39, |v119|
	v_add_f32_e64 v38, v38, |v120|
	v_add_f32_e64 v39, v39, |v121|
	v_add_f32_e64 v38, v38, |v122|
	v_add_f32_e64 v39, v39, |v123|
	v_add_f32_e64 v38, v38, |v124|
	v_add_f32_e32 v25, v38, v39
	v_mfma_f32_32x32x16_f16 v[112:127], v[32:35], v[76:79], 0
	v_add_f32_e64 v38, |v96|, |v97|
	v_add_f32_e64 v39, |v98|, |v99|
	v_add_f32_e64 v38, v38, |v100|
	v_add_f32_e64 v39, v39, |v101|
	v_add_f32_e64 v38, v38, |v102|
	v_add_f32_e64 v39, v39, |v103|
	v_add_f32_e64 v38, v38, |v104|
	v_add_f32_e64 v39, v39, |v105|
	v_add_f32_e64 v38, v38, |v106|
	v_add_f32_e64 v39, v39, |v107|
	v_add_f32_e64 v38, v38, |v108|
	v_add_f32_e32 v26, v38, v39
	v_mfma_f32_32x32x16_f16 v[96:111], v[32:35], v[80:83], 0
	v_add_f32_e64 v38, |v112|, |v113|
	v_add_f32_e64 v39, |v114|, |v115|
	v_add_f32_e64 v38, v38, |v116|
	v_add_f32_e64 v39, v39, |v117|
	v_add_f32_e64 v38, v38, |v118|
	v_add_f32_e64 v39, v39, |v119|
	v_add_f32_e64 v38, v38, |v120|
	v_add_f32_e64 v39, v39, |v121|
	v_add_f32_e64 v38, v38, |v122|
	v_add_f32_e64 v39, v39, |v123|
	v_add_f32_e64 v38, v38, |v124|
	v_add_f32_e32 v27, v38, v39
	v_mfma_f32_32x32x16_f16 v[112:127], v[32:35], v[84:87], 0
	v_add_f32_e64 v38, |v96|, |v97|
	v_add_f32_e64 v39, |v98|, |v99|
	v_add_f32_e64 v38, v38, |v100|
	v_add_f32_e64 v39, v39, |v101|
	v_add_f32_e64 v38, v38, |v102|
	v_add_f32_e64 v39, v39, |v103|
	v_add_f32_e64 v38, v38, |v104|
	v_add_f32_e64 v39, v39, |v105|
	v_add_f32_e64 v38, v38, |v106|
	v_add_f32_e64 v39, v39, |v107|
	v_add_f32_e64 v38, v38, |v108|
	v_add_f32_e32 v28, v38, v39
	v_mfma_f32_32x32x16_f16 v[96:111], v[32:35], v[88:91], 0
	v_add_f32_e64 v38, |v112|, |v113|
	v_add_f32_e64 v39, |v114|, |v115|
	v_add_f32_e64 v38, v38, |v116|
	v_add_f32_e64 v39, v39, |v117|
	v_add_f32_e64 v38, v38, |v118|
	v_add_f32_e64 v39, v39, |v119|
	v_add_f32_e64 v38, v38, |v120|
	v_add_f32_e64 v39, v39, |v121|
	v_add_f32_e64 v38, v38, |v122|
	v_add_f32_e64 v39, v39, |v123|
	v_add_f32_e64 v38, v38, |v124|
	v_add_f32_e32 v29, v38, v39
	v_mfma_f32_32x32x16_f16 v[112:127], v[32:35], v[92:95], 0
	v_add_f32_e64 v38, |v96|, |v97|
	v_add_f32_e64 v39, |v98|, |v99|
	v_add_f32_e64 v38, v38, |v100|
	v_add_f32_e64 v39, v39, |v101|
	v_add_f32_e64 v38, v38, |v102|
	v_add_f32_e64 v39, v39, |v103|
	v_add_f32_e64 v38, v38, |v104|
	v_add_f32_e64 v39, v39, |v105|
	v_add_f32_e64 v38, v38, |v106|
	v_add_f32_e64 v39, v39, |v107|
	v_add_f32_e64 v38, v38, |v108|
	v_add_f32_e32 v30, v38, v39
	v_add_f32_e64 v38, |v112|, |v113|
	v_add_f32_e64 v39, |v114|, |v115|
	v_add_f32_e64 v38, v38, |v116|
	v_add_f32_e64 v39, v39, |v117|
	v_add_f32_e64 v38, v38, |v118|
	v_add_f32_e64 v39, v39, |v119|
	v_add_f32_e64 v38, v38, |v120|
	v_add_f32_e64 v39, v39, |v121|
	v_add_f32_e64 v38, v38, |v122|
	v_add_f32_e64 v39, v39, |v123|
	v_add_f32_e64 v38, v38, |v124|
	v_add_f32_e32 v31, v38, v39
	s_branch .Lafter_first
.Lf14:
	v_add_f32_e64 v38, |v96|, |v97|
	v_add_f32_e64 v39, |v98|, |v99|
	v_add_f32_e64 v38, v38, |v100|
	v_add_f32_e64 v39, v39, |v101|
	v_add_f32_e64 v38, v38, |v102|
	v_add_f32_e64 v39, v39, |v103|
	v_add_f32_e64 v38, v38, |v104|
	v_add_f32_e64 v39, v39, |v105|
	v_add_f32_e64 v38, v38, |v106|
	v_add_f32_e64 v39, v39, |v107|
	v_add_f32_e64 v38, v38, |v108|
	v_add_f32_e64 v39, v39, |v109|
	v_add_f32_e32 v24, v38, v39
	v_mfma_f32_32x32x16_f16 v[96:111], v[32:35], v[72:75], 0
	v_add_f32_e64 v38, |v112|, |v113|
	v_add_f32_e64 v39, |v114|, |v115|
	v_add_f32_e64 v38, v38, |v116|
	v_add_f32_e64 v39, v39, |v117|
	v_add_f32_e64 v38, v38, |v118|
	v_add_f32_e64 v39, v39, |v119|
	v_add_f32_e64 v38, v38, |v120|
	v_add_f32_e64 v39, v39, |v121|
	v_add_f32_e64 v38, v38, |v122|
	v_add_f32_e64 v39, v39, |v123|
	v_add_f32_e64 v38, v38, |v124|
	v_add_f32_e64 v39, v39, |v125|
	v_add_f32_e32 v25, v38, v39
	v_mfma_f32_32x32x16_f16 v[112:127], v[32:35], v[76:79], 0
	v_add_f32_e64 v38, |v96|, |v97|
	v_add_f32_e64 v39, |v98|, |v99|
	v_add_f32_e64 v38, v38, |v100|
	v_add_f32_e64 v39, v39, |v101|
	v_add_f32_e64 v38, v38, |v102|
	v_add_f32_e64 v39, v39, |v103|
	v_add_f32_e64 v38, v38, |v104|
	v_add_f32_e64 v39, v39, |v105|
	v_add_f32_e64 v38, v38, |v106|
	v_add_f32_e64 v39, v39, |v107|
	v_add_f32_e64 v38, v38, |v108|
	v_add_f32_e64 v39, v39, |v109|
	v_add_f32_e32 v26, v38, v39
	v_mfma_f32_32x32x16_f16 v[96:111], v[32:35], v[80:83], 0
	v_add_f32_e64 v38, |v112|, |v113|
	v_add_f32_e64 v39, |v114|, |v115|
	v_add_f32_e64 v38, v38, |v116|
	v_add_f32_e64 v39, v39, |v117|
	v_add_f32_e64 v38, v38, |v118|
	v_add_f32_e64 v39, v39, |v119|
	v_add_f32_e64 v38, v38, |v120|
	v_add_f32_e64 v39, v39, |v121|
	v_add_f32_e64 v38, v38, |v122|
	v_add_f32_e64 v39, v39, |v123|
	v_add_f32_e64 v38, v38, |v124|
	v_add_f32_e64 v39, v39, |v125|
	v_add_f32_e32 v27, v38, v39
	v_mfma_f32_32x32x16_f16 v[112:127], v[32:35], v[84:87], 0
	v_add_f32_e64 v38, |v96|, |v97|
	v_add_f32_e64 v39, |v98|, |v99|
	v_add_f32_e64 v38, v38, |v100|
	v_add_f32_e64 v39, v39, |v101|
	v_add_f32_e64 v38, v38, |v102|
	v_add_f32_e64 v39, v39, |v103|
	v_add_f32_e64 v38, v38, |v104|
	v_add_f32_e64 v39, v39, |v105|
	v_add_f32_e64 v38, v38, |v106|
	v_add_f32_e64 v39, v39, |v107|
	v_add_f32_e64 v38, v38, |v108|
	v_add_f32_e64 v39, v39, |v109|
	v_add_f32_e32 v28, v38, v39
	v_mfma_f32_32x32x16_f16 v[96:111], v[32:35], v[88:91], 0
	v_add_f32_e64 v38, |v112|, |v113|
	v_add_f32_e64 v39, |v114|, |v115|
	v_add_f32_e64 v38, v38, |v116|
	v_add_f32_e64 v39, v39, |v117|
	v_add_f32_e64 v38, v38, |v118|
	v_add_f32_e64 v39, v39, |v119|
	v_add_f32_e64 v38, v38, |v120|
	v_add_f32_e64 v39, v39, |v121|
	v_add_f32_e64 v38, v38, |v122|
	v_add_f32_e64 v39, v39, |v123|
	v_add_f32_e64 v38, v38, |v124|
	v_add_f32_e64 v39, v39, |v125|
	v_add_f32_e32 v29, v38, v39
	v_mfma_f32_32x32x16_f16 v[112:127], v[32:35], v[92:95], 0
	v_add_f32_e64 v38, |v96|, |v97|
	v_add_f32_e64 v39, |v98|, |v99|
	v_add_f32_e64 v38, v38, |v100|
	v_add_f32_e64 v39, v39, |v101|
	v_add_f32_e64 v38, v38, |v102|
	v_add_f32_e64 v39, v39, |v103|
	v_add_f32_e64 v38, v38, |v104|
	v_add_f32_e64 v39, v39, |v105|
	v_add_f32_e64 v38, v38, |v106|
	v_add_f32_e64 v39, v39, |v107|
	v_add_f32_e64 v38, v38, |v108|
	v_add_f32_e64 v39, v39, |v109|
	v_add_f32_e32 v30, v38, v39
	v_add_f32_e64 v38, |v112|, |v113|
	v_add_f32_e64 v39, |v114|, |v115|
	v_add_f32_e64 v38, v38, |v116|
	v_add_f32_e64 v39, v39, |v117|
	v_add_f32_e64 v38, v38, |v118|
	v_add_f32_e64 v39, v39, |v119|
	v_add_f32_e64 v38, v38, |v120|
	v_add_f32_e64 v39, v39, |v121|
	v_add_f32_e64 v38, v38, |v122|
	v_add_f32_e64 v39, v39, |v123|
	v_add_f32_e64 v38, v38, |v124|
	v_add_f32_e64 v39, v39, |v125|
	v_add_f32_e32 v31, v38, v39
	s_branch .Lafter_first
.Lf15:
	v_add_f32_e64 v38, |v96|, |v97|
	v_add_f32_e64 v39, |v98|, |v99|
	v_add_f32_e64 v38, v38, |v100|
	v_add_f32_e64 v39, v39, |v101|
	v_add_f32_e64 v38, v38, |v102|
	v_add_f32_e64 v39, v39, |v103|
	v_add_f32_e64 v38, v38, |v104|
	v_add_f32_e64 v39, v39, |v105|
	v_add_f32_e64 v38, v38, |v106|
	v_add_f32_e64 v39, v39, |v107|
	v_add_f32_e64 v38, v38, |v108|
	v_add_f32_e64 v39, v39, |v109|
	v_add_f32_e64 v38, v38, |v110|
	v_add_f32_e32 v24, v38, v39
	v_mfma_f32_32x32x16_f16 v[96:111], v[32:35], v[72:75], 0
	v_add_f32_e64 v38, |v112|, |v113|
	v_add_f32_e64 v39, |v114|, |v115|
	v_add_f32_e64 v38, v38, |v116|
	v_add_f32_e64 v39, v39, |v117|
	v_add_f32_e64 v38, v38, |v118|
	v_add_f32_e64 v39, v39, |v119|
	v_add_f32_e64 v38, v38, |v120|
	v_add_f32_e64 v39, v39, |v121|
	v_add_f32_e64 v38, v38, |v122|
	v_add_f32_e64 v39, v39, |v123|
	v_add_f32_e64 v38, v38, |v124|
	v_add_f32_e64 v39, v39, |v125|
	v_add_f32_e64 v38, v38, |v126|
	v_add_f32_e32 v25, v38, v39
	v_mfma_f32_32x32x16_f16 v[112:127], v[32:35], v[76:79], 0
	v_add_f32_e64 v38, |v96|, |v97|
	v_add_f32_e64 v39, |v98|, |v99|
	v_add_f32_e64 v38, v38, |v100|
	v_add_f32_e64 v39, v39, |v101|
	v_add_f32_e64 v38, v38, |v102|
	v_add_f32_e64 v39, v39, |v103|
	v_add_f32_e64 v38, v38, |v104|
	v_add_f32_e64 v39, v39, |v105|
	v_add_f32_e64 v38, v38, |v106|
	v_add_f32_e64 v39, v39, |v107|
	v_add_f32_e64 v38, v38, |v108|
	v_add_f32_e64 v39, v39, |v109|
	v_add_f32_e64 v38, v38, |v110|
	v_add_f32_e32 v26, v38, v39
	v_mfma_f32_32x32x16_f16 v[96:111], v[32:35], v[80:83], 0
	v_add_f32_e64 v38, |v112|, |v113|
	v_add_f32_e64 v39, |v114|, |v115|
	v_add_f32_e64 v38, v38, |v116|
	v_add_f32_e64 v39, v39, |v117|
	v_add_f32_e64 v38, v38, |v118|
	v_add_f32_e64 v39, v39, |v119|
	v_add_f32_e64 v38, v38, |v120|
	v_add_f32_e64 v39, v39, |v121|
	v_add_f32_e64 v38, v38, |v122|
	v_add_f32_e64 v39, v39, |v123|
	v_add_f32_e64 v38, v38, |v124|
	v_add_f32_e64 v39, v39, |v125|
	v_add_f32_e64 v38, v38, |v126|
	v_add_f32_e32 v27, v38, v39
	v_mfma_f32_32x32x16_f16 v[112:127], v[32:35], v[84:87], 0
	v_add_f32_e64 v38, |v96|, |v97|
	v_add_f32_e64 v39, |v98|, |v99|
	v_add_f32_e64 v38, v38, |v100|
	v_add_f32_e64 v39, v39, |v101|
	v_add_f32_e64 v38, v38, |v102|
	v_add_f32_e64 v39, v39, |v103|
	v_add_f32_e64 v38, v38, |v104|
	v_add_f32_e64 v39, v39, |v105|
	v_add_f32_e64 v38, v38, |v106|
	v_add_f32_e64 v39, v39, |v107|
	v_add_f32_e64 v38, v38, |v108|
	v_add_f32_e64 v39, v39, |v109|
	v_add_f32_e64 v38, v38, |v110|
	v_add_f32_e32 v28, v38, v39
	v_mfma_f32_32x32x16_f16 v[96:111], v[32:35], v[88:91], 0
	v_add_f32_e64 v38, |v112|, |v113|
	v_add_f32_e64 v39, |v114|, |v115|
	v_add_f32_e64 v38, v38, |v116|
	v_add_f32_e64 v39, v39, |v117|
	v_add_f32_e64 v38, v38, |v118|
	v_add_f32_e64 v39, v39, |v119|
	v_add_f32_e64 v38, v38, |v120|
	v_add_f32_e64 v39, v39, |v121|
	v_add_f32_e64 v38, v38, |v122|
	v_add_f32_e64 v39, v39, |v123|
	v_add_f32_e64 v38, v38, |v124|
	v_add_f32_e64 v39, v39, |v125|
	v_add_f32_e64 v38, v38, |v126|
	v_add_f32_e32 v29, v38, v39
	v_mfma_f32_32x32x16_f16 v[112:127], v[32:35], v[92:95], 0
	v_add_f32_e64 v38, |v96|, |v97|
	v_add_f32_e64 v39, |v98|, |v99|
	v_add_f32_e64 v38, v38, |v100|
	v_add_f32_e64 v39, v39, |v101|
	v_add_f32_e64 v38, v38, |v102|
	v_add_f32_e64 v39, v39, |v103|
	v_add_f32_e64 v38, v38, |v104|
	v_add_f32_e64 v39, v39, |v105|
	v_add_f32_e64 v38, v38, |v106|
	v_add_f32_e64 v39, v39, |v107|
	v_add_f32_e64 v38, v38, |v108|
	v_add_f32_e64 v39, v39, |v109|
	v_add_f32_e64 v38, v38, |v110|
	v_add_f32_e32 v30, v38, v39
	v_add_f32_e64 v38, |v112|, |v113|
	v_add_f32_e64 v39, |v114|, |v115|
	v_add_f32_e64 v38, v38, |v116|
	v_add_f32_e64 v39, v39, |v117|
	v_add_f32_e64 v38, v38, |v118|
	v_add_f32_e64 v39, v39, |v119|
	v_add_f32_e64 v38, v38, |v120|
	v_add_f32_e64 v39, v39, |v121|
	v_add_f32_e64 v38, v38, |v122|
	v_add_f32_e64 v39, v39, |v123|
	v_add_f32_e64 v38, v38, |v124|
	v_add_f32_e64 v39, v39, |v125|
	v_add_f32_e64 v38, v38, |v126|
	v_add_f32_e32 v31, v38, v39
	s_branch .Lafter_first

.Lsub:
	ds_read_b64 v[36:37], v2
	v_cmp_gt_u32_e32 vcc, v3, v8
	v_add_u32_e32 v2, 64, v2
	v_add_u32_e32 v8, 16, v8
	v_mov_b32_e32 v33, 0x3c00
	s_waitcnt lgkmcnt(0)
	v_perm_b32 v32, v37, v36, v57
	v_cndmask_b32_e32 v33, 0, v33, vcc
	s_nop 0
	v_cndmask_b32_e32 v32, 0, v32, vcc
	s_nop 1
	v_mfma_f32_32x32x16_f16 v[96:111], v[32:35], v[64:67], 0
	v_mfma_f32_32x32x16_f16 v[112:127], v[32:35], v[68:71], 0
	s_nop 10
	s_sub_u32 s45, s43, s44
	s_min_u32 s46, s45, 16
	s_cmp_eq_u32 s46, 2
	s_cbranch_scc1 .Ln2
	s_cmp_eq_u32 s46, 3
	s_cbranch_scc1 .Ln3
	s_cmp_eq_u32 s46, 4
	s_cbranch_scc1 .Ln4
	s_cmp_eq_u32 s46, 5
	s_cbranch_scc1 .Ln5
	s_cmp_eq_u32 s46, 6
	s_cbranch_scc1 .Ln6
	s_cmp_eq_u32 s46, 7
	s_cbranch_scc1 .Ln7
	s_cmp_eq_u32 s46, 8
	s_cbranch_scc1 .Ln8
	s_cmp_eq_u32 s46, 9
	s_cbranch_scc1 .Ln9
	s_cmp_eq_u32 s46, 10
	s_cbranch_scc1 .Ln10
	s_cmp_eq_u32 s46, 11
	s_cbranch_scc1 .Ln11
	s_cmp_eq_u32 s46, 12
	s_cbranch_scc1 .Ln12
	s_cmp_eq_u32 s46, 13
	s_cbranch_scc1 .Ln13
	s_cmp_eq_u32 s46, 14
	s_cbranch_scc1 .Ln14
	s_cmp_eq_u32 s46, 15
	s_cbranch_scc1 .Ln15
	s_cmp_eq_u32 s46, 16
	s_cbranch_scc1 .Ln16
.Ln1:
	v_add_f32_e64 v24, v24, |v96|
	s_nop 10
	v_mfma_f32_32x32x16_f16 v[96:111], v[32:35], v[72:75], 0
	v_add_f32_e64 v25, v25, |v112|
	s_nop 10
	v_mfma_f32_32x32x16_f16 v[112:127], v[32:35], v[76:79], 0
	v_add_f32_e64 v26, v26, |v96|
	s_nop 10
	v_mfma_f32_32x32x16_f16 v[96:111], v[32:35], v[80:83], 0
	v_add_f32_e64 v27, v27, |v112|
	s_nop 10
	v_mfma_f32_32x32x16_f16 v[112:127], v[32:35], v[84:87], 0
	v_add_f32_e64 v28, v28, |v96|
	s_nop 10
	v_mfma_f32_32x32x16_f16 v[96:111], v[32:35], v[88:91], 0
	v_add_f32_e64 v29, v29, |v112|
	s_nop 10
	v_mfma_f32_32x32x16_f16 v[112:127], v[32:35], v[92:95], 0
	v_add_f32_e64 v30, v30, |v96|
	s_nop 10
	v_add_f32_e64 v31, v31, |v112|
	s_nop 10
	s_branch .Lsub_next
.Ln2:
	v_add_f32_e64 v38, |v96|, |v97|
	v_add_f32_e32 v24, v24, v38
	s_nop 9
	v_mfma_f32_32x32x16_f16 v[96:111], v[32:35], v[72:75], 0
	v_add_f32_e64 v38, |v112|, |v113|
	v_add_f32_e32 v25, v25, v38
	s_nop 9
	v_mfma_f32_32x32x16_f16 v[112:127], v[32:35], v[76:79], 0
	v_add_f32_e64 v38, |v96|, |v97|
	v_add_f32_e32 v26, v26, v38
	s_nop 9
	v_mfma_f32_32x32x16_f16 v[96:111], v[32:35], v[80:83], 0
	v_add_f32_e64 v38, |v112|, |v113|
	v_add_f32_e32 v27, v27, v38
	s_nop 9
	v_mfma_f32_32x32x16_f16 v[112:127], v[32:35], v[84:87], 0
	v_add_f32_e64 v38, |v96|, |v97|
	v_add_f32_e32 v28, v28, v38
	s_nop 9
	v_mfma_f32_32x32x16_f16 v[96:111], v[32:35], v[88:91], 0
	v_add_f32_e64 v38, |v112|, |v113|
	v_add_f32_e32 v29, v29, v38
	s_nop 9
	v_mfma_f32_32x32x16_f16 v[112:127], v[32:35], v[92:95], 0
	v_add_f32_e64 v38, |v96|, |v97|
	v_add_f32_e32 v30, v30, v38
	s_nop 9
	v_add_f32_e64 v38, |v112|, |v113|
	v_add_f32_e32 v31, v31, v38
	s_nop 9
	s_branch .Lsub_next
.Ln3:
	v_add_f32_e64 v38, |v96|, |v97|
	v_add_f32_e64 v24, v24, |v98|
	v_add_f32_e32 v24, v24, v38
	s_nop 8
	v_mfma_f32_32x32x16_f16 v[96:111], v[32:35], v[72:75], 0
	v_add_f32_e64 v38, |v112|, |v113|
	v_add_f32_e64 v25, v25, |v114|
	v_add_f32_e32 v25, v25, v38
	s_nop 8
	v_mfma_f32_32x32x16_f16 v[112:127], v[32:35], v[76:79], 0
	v_add_f32_e64 v38, |v96|, |v97|
	v_add_f32_e64 v26, v26, |v98|
	v_add_f32_e32 v26, v26, v38
	s_nop 8
	v_mfma_f32_32x32x16_f16 v[96:111], v[32:35], v[80:83], 0
	v_add_f32_e64 v38, |v112|, |v113|
	v_add_f32_e64 v27, v27, |v114|
	v_add_f32_e32 v27, v27, v38
	s_nop 8
	v_mfma_f32_32x32x16_f16 v[112:127], v[32:35], v[84:87], 0
	v_add_f32_e64 v38, |v96|, |v97|
	v_add_f32_e64 v28, v28, |v98|
	v_add_f32_e32 v28, v28, v38
	s_nop 8
	v_mfma_f32_32x32x16_f16 v[96:111], v[32:35], v[88:91], 0
	v_add_f32_e64 v38, |v112|, |v113|
	v_add_f32_e64 v29, v29, |v114|
	v_add_f32_e32 v29, v29, v38
	s_nop 8
	v_mfma_f32_32x32x16_f16 v[112:127], v[32:35], v[92:95], 0
	v_add_f32_e64 v38, |v96|, |v97|
	v_add_f32_e64 v30, v30, |v98|
	v_add_f32_e32 v30, v30, v38
	s_nop 8
	v_add_f32_e64 v38, |v112|, |v113|
	v_add_f32_e64 v31, v31, |v114|
	v_add_f32_e32 v31, v31, v38
	s_nop 8
	s_branch .Lsub_next

.Ln5:
	v_add_f32_e64 v38, |v96|, |v97|
	v_add_f32_e64 v39, |v98|, |v99|
	v_add_f32_e64 v38, v38, |v100|
	v_add_f32_e32 v38, v38, v39
	v_add_f32_e32 v24, v24, v38
	s_nop 6
	v_mfma_f32_32x32x16_f16 v[96:111], v[32:35], v[72:75], 0
	v_add_f32_e64 v38, |v112|, |v113|
	v_add_f32_e64 v39, |v114|, |v115|
	v_add_f32_e64 v38, v38, |v116|
	v_add_f32_e32 v38, v38, v39
	v_add_f32_e32 v25, v25, v38
	s_nop 6
	v_mfma_f32_32x32x16_f16 v[112:127], v[32:35], v[76:79], 0
	v_add_f32_e64 v38, |v96|, |v97|
	v_add_f32_e64 v39, |v98|, |v99|
	v_add_f32_e64 v38, v38, |v100|
	v_add_f32_e32 v38, v38, v39
	v_add_f32_e32 v26, v26, v38
	s_nop 6
	v_mfma_f32_32x32x16_f16 v[96:111], v[32:35], v[80:83], 0
	v_add_f32_e64 v38, |v112|, |v113|
	v_add_f32_e64 v39, |v114|, |v115|
	v_add_f32_e64 v38, v38, |v116|
	v_add_f32_e32 v38, v38, v39
	v_add_f32_e32 v27, v27, v38
	s_nop 6
	v_mfma_f32_32x32x16_f16 v[112:127], v[32:35], v[84:87], 0
	v_add_f32_e64 v38, |v96|, |v97|
	v_add_f32_e64 v39, |v98|, |v99|
	v_add_f32_e64 v38, v38, |v100|
	v_add_f32_e32 v38, v38, v39
	v_add_f32_e32 v28, v28, v38
	s_nop 6
	v_mfma_f32_32x32x16_f16 v[96:111], v[32:35], v[88:91], 0
	v_add_f32_e64 v38, |v112|, |v113|
	v_add_f32_e64 v39, |v114|, |v115|
	v_add_f32_e64 v38, v38, |v116|
	v_add_f32_e32 v38, v38, v39
	v_add_f32_e32 v29, v29, v38
	s_nop 6
	v_mfma_f32_32x32x16_f16 v[112:127], v[32:35], v[92:95], 0
	v_add_f32_e64 v38, |v96|, |v97|
	v_add_f32_e64 v39, |v98|, |v99|
	v_add_f32_e64 v38, v38, |v100|
	v_add_f32_e32 v38, v38, v39
	v_add_f32_e32 v30, v30, v38
	s_nop 6
	v_add_f32_e64 v38, |v112|, |v113|
	v_add_f32_e64 v39, |v114|, |v115|
	v_add_f32_e64 v38, v38, |v116|
	v_add_f32_e32 v38, v38, v39
	v_add_f32_e32 v31, v31, v38
	s_nop 6
	s_branch .Lsub_next
.Ln6:
	v_add_f32_e64 v38, |v96|, |v97|
	v_add_f32_e64 v39, |v98|, |v99|
	v_add_f32_e64 v38, v38, |v100|
	v_add_f32_e64 v39, v39, |v101|
	v_add_f32_e32 v38, v38, v39
	v_add_f32_e32 v24, v24, v38
	s_nop 5
	v_mfma_f32_32x32x16_f16 v[96:111], v[32:35], v[72:75], 0
	v_add_f32_e64 v38, |v112|, |v113|
	v_add_f32_e64 v39, |v114|, |v115|
	v_add_f32_e64 v38, v38, |v116|
	v_add_f32_e64 v39, v39, |v117|
	v_add_f32_e32 v38, v38, v39
	v_add_f32_e32 v25, v25, v38
	s_nop 5
	v_mfma_f32_32x32x16_f16 v[112:127], v[32:35], v[76:79], 0
	v_add_f32_e64 v38, |v96|, |v97|
	v_add_f32_e64 v39, |v98|, |v99|
	v_add_f32_e64 v38, v38, |v100|
	v_add_f32_e64 v39, v39, |v101|
	v_add_f32_e32 v38, v38, v39
	v_add_f32_e32 v26, v26, v38
	s_nop 5
	v_mfma_f32_32x32x16_f16 v[96:111], v[32:35], v[80:83], 0
	v_add_f32_e64 v38, |v112|, |v113|
	v_add_f32_e64 v39, |v114|, |v115|
	v_add_f32_e64 v38, v38, |v116|
	v_add_f32_e64 v39, v39, |v117|
	v_add_f32_e32 v38, v38, v39
	v_add_f32_e32 v27, v27, v38
	s_nop 5
	v_mfma_f32_32x32x16_f16 v[112:127], v[32:35], v[84:87], 0
	v_add_f32_e64 v38, |v96|, |v97|
	v_add_f32_e64 v39, |v98|, |v99|
	v_add_f32_e64 v38, v38, |v100|
	v_add_f32_e64 v39, v39, |v101|
	v_add_f32_e32 v38, v38, v39
	v_add_f32_e32 v28, v28, v38
	s_nop 5
	v_mfma_f32_32x32x16_f16 v[96:111], v[32:35], v[88:91], 0
	v_add_f32_e64 v38, |v112|, |v113|
	v_add_f32_e64 v39, |v114|, |v115|
	v_add_f32_e64 v38, v38, |v116|
	v_add_f32_e64 v39, v39, |v117|
	v_add_f32_e32 v38, v38, v39
	v_add_f32_e32 v29, v29, v38
	s_nop 5
	v_mfma_f32_32x32x16_f16 v[112:127], v[32:35], v[92:95], 0
	v_add_f32_e64 v38, |v96|, |v97|
	v_add_f32_e64 v39, |v98|, |v99|
	v_add_f32_e64 v38, v38, |v100|
	v_add_f32_e64 v39, v39, |v101|
	v_add_f32_e32 v38, v38, v39
	v_add_f32_e32 v30, v30, v38
	s_nop 5
	v_add_f32_e64 v38, |v112|, |v113|
	v_add_f32_e64 v39, |v114|, |v115|
	v_add_f32_e64 v38, v38, |v116|
	v_add_f32_e64 v39, v39, |v117|
	v_add_f32_e32 v38, v38, v39
	v_add_f32_e32 v31, v31, v38
	s_nop 5
	s_branch .Lsub_next
.Ln7:
	v_add_f32_e64 v38, |v96|, |v97|
	v_add_f32_e64 v39, |v98|, |v99|
	v_add_f32_e64 v38, v38, |v100|
	v_add_f32_e64 v39, v39, |v101|
	v_add_f32_e64 v38, v38, |v102|
	v_add_f32_e32 v38, v38, v39
	v_add_f32_e32 v24, v24, v38
	s_nop 4
	v_mfma_f32_32x32x16_f16 v[96:111], v[32:35], v[72:75], 0
	v_add_f32_e64 v38, |v112|, |v113|
	v_add_f32_e64 v39, |v114|, |v115|
	v_add_f32_e64 v38, v38, |v116|
	v_add_f32_e64 v39, v39, |v117|
	v_add_f32_e64 v38, v38, |v118|
	v_add_f32_e32 v38, v38, v39
	v_add_f32_e32 v25, v25, v38
	s_nop 4
	v_mfma_f32_32x32x16_f16 v[112:127], v[32:35], v[76:79], 0
	v_add_f32_e64 v38, |v96|, |v97|
	v_add_f32_e64 v39, |v98|, |v99|
	v_add_f32_e64 v38, v38, |v100|
	v_add_f32_e64 v39, v39, |v101|
	v_add_f32_e64 v38, v38, |v102|
	v_add_f32_e32 v38, v38, v39
	v_add_f32_e32 v26, v26, v38
	s_nop 4
	v_mfma_f32_32x32x16_f16 v[96:111], v[32:35], v[80:83], 0
	v_add_f32_e64 v38, |v112|, |v113|
	v_add_f32_e64 v39, |v114|, |v115|
	v_add_f32_e64 v38, v38, |v116|
	v_add_f32_e64 v39, v39, |v117|
	v_add_f32_e64 v38, v38, |v118|
	v_add_f32_e32 v38, v38, v39
	v_add_f32_e32 v27, v27, v38
	s_nop 4
	v_mfma_f32_32x32x16_f16 v[112:127], v[32:35], v[84:87], 0
	v_add_f32_e64 v38, |v96|, |v97|
	v_add_f32_e64 v39, |v98|, |v99|
	v_add_f32_e64 v38, v38, |v100|
	v_add_f32_e64 v39, v39, |v101|
	v_add_f32_e64 v38, v38, |v102|
	v_add_f32_e32 v38, v38, v39
	v_add_f32_e32 v28, v28, v38
	s_nop 4
	v_mfma_f32_32x32x16_f16 v[96:111], v[32:35], v[88:91], 0
	v_add_f32_e64 v38, |v112|, |v113|
	v_add_f32_e64 v39, |v114|, |v115|
	v_add_f32_e64 v38, v38, |v116|
	v_add_f32_e64 v39, v39, |v117|
	v_add_f32_e64 v38, v38, |v118|
	v_add_f32_e32 v38, v38, v39
	v_add_f32_e32 v29, v29, v38
	s_nop 4
	v_mfma_f32_32x32x16_f16 v[112:127], v[32:35], v[92:95], 0
	v_add_f32_e64 v38, |v96|, |v97|
	v_add_f32_e64 v39, |v98|, |v99|
	v_add_f32_e64 v38, v38, |v100|
	v_add_f32_e64 v39, v39, |v101|
	v_add_f32_e64 v38, v38, |v102|
	v_add_f32_e32 v38, v38, v39
	v_add_f32_e32 v30, v30, v38
	s_nop 4
	v_add_f32_e64 v38, |v112|, |v113|
	v_add_f32_e64 v39, |v114|, |v115|
	v_add_f32_e64 v38, v38, |v116|
	v_add_f32_e64 v39, v39, |v117|
	v_add_f32_e64 v38, v38, |v118|
	v_add_f32_e32 v38, v38, v39
	v_add_f32_e32 v31, v31, v38
	s_nop 4
	s_branch .Lsub_next

.Ln9:
	v_add_f32_e64 v38, |v96|, |v97|
	v_add_f32_e64 v39, |v98|, |v99|
	v_add_f32_e64 v38, v38, |v100|
	v_add_f32_e64 v39, v39, |v101|
	v_add_f32_e64 v38, v38, |v102|
	v_add_f32_e64 v39, v39, |v103|
	v_add_f32_e64 v38, v38, |v104|
	v_add_f32_e32 v38, v38, v39
	v_add_f32_e32 v24, v24, v38
	s_nop 2
	v_mfma_f32_32x32x16_f16 v[96:111], v[32:35], v[72:75], 0
	v_add_f32_e64 v38, |v112|, |v113|
	v_add_f32_e64 v39, |v114|, |v115|
	v_add_f32_e64 v38, v38, |v116|
	v_add_f32_e64 v39, v39, |v117|
	v_add_f32_e64 v38, v38, |v118|
	v_add_f32_e64 v39, v39, |v119|
	v_add_f32_e64 v38, v38, |v120|
	v_add_f32_e32 v38, v38, v39
	v_add_f32_e32 v25, v25, v38
	s_nop 2
	v_mfma_f32_32x32x16_f16 v[112:127], v[32:35], v[76:79], 0
	v_add_f32_e64 v38, |v96|, |v97|
	v_add_f32_e64 v39, |v98|, |v99|
	v_add_f32_e64 v38, v38, |v100|
	v_add_f32_e64 v39, v39, |v101|
	v_add_f32_e64 v38, v38, |v102|
	v_add_f32_e64 v39, v39, |v103|
	v_add_f32_e64 v38, v38, |v104|
	v_add_f32_e32 v38, v38, v39
	v_add_f32_e32 v26, v26, v38
	s_nop 2
	v_mfma_f32_32x32x16_f16 v[96:111], v[32:35], v[80:83], 0
	v_add_f32_e64 v38, |v112|, |v113|
	v_add_f32_e64 v39, |v114|, |v115|
	v_add_f32_e64 v38, v38, |v116|
	v_add_f32_e64 v39, v39, |v117|
	v_add_f32_e64 v38, v38, |v118|
	v_add_f32_e64 v39, v39, |v119|
	v_add_f32_e64 v38, v38, |v120|
	v_add_f32_e32 v38, v38, v39
	v_add_f32_e32 v27, v27, v38
	s_nop 2
	v_mfma_f32_32x32x16_f16 v[112:127], v[32:35], v[84:87], 0
	v_add_f32_e64 v38, |v96|, |v97|
	v_add_f32_e64 v39, |v98|, |v99|
	v_add_f32_e64 v38, v38, |v100|
	v_add_f32_e64 v39, v39, |v101|
	v_add_f32_e64 v38, v38, |v102|
	v_add_f32_e64 v39, v39, |v103|
	v_add_f32_e64 v38, v38, |v104|
	v_add_f32_e32 v38, v38, v39
	v_add_f32_e32 v28, v28, v38
	s_nop 2
	v_mfma_f32_32x32x16_f16 v[96:111], v[32:35], v[88:91], 0
	v_add_f32_e64 v38, |v112|, |v113|
	v_add_f32_e64 v39, |v114|, |v115|
	v_add_f32_e64 v38, v38, |v116|
	v_add_f32_e64 v39, v39, |v117|
	v_add_f32_e64 v38, v38, |v118|
	v_add_f32_e64 v39, v39, |v119|
	v_add_f32_e64 v38, v38, |v120|
	v_add_f32_e32 v38, v38, v39
	v_add_f32_e32 v29, v29, v38
	s_nop 2
	v_mfma_f32_32x32x16_f16 v[112:127], v[32:35], v[92:95], 0
	v_add_f32_e64 v38, |v96|, |v97|
	v_add_f32_e64 v39, |v98|, |v99|
	v_add_f32_e64 v38, v38, |v100|
	v_add_f32_e64 v39, v39, |v101|
	v_add_f32_e64 v38, v38, |v102|
	v_add_f32_e64 v39, v39, |v103|
	v_add_f32_e64 v38, v38, |v104|
	v_add_f32_e32 v38, v38, v39
	v_add_f32_e32 v30, v30, v38
	s_nop 2
	v_add_f32_e64 v38, |v112|, |v113|
	v_add_f32_e64 v39, |v114|, |v115|
	v_add_f32_e64 v38, v38, |v116|
	v_add_f32_e64 v39, v39, |v117|
	v_add_f32_e64 v38, v38, |v118|
	v_add_f32_e64 v39, v39, |v119|
	v_add_f32_e64 v38, v38, |v120|
	v_add_f32_e32 v38, v38, v39
	v_add_f32_e32 v31, v31, v38
	s_nop 2
	s_branch .Lsub_next
.Ln10:
	v_add_f32_e64 v38, |v96|, |v97|
	v_add_f32_e64 v39, |v98|, |v99|
	v_add_f32_e64 v38, v38, |v100|
	v_add_f32_e64 v39, v39, |v101|
	v_add_f32_e64 v38, v38, |v102|
	v_add_f32_e64 v39, v39, |v103|
	v_add_f32_e64 v38, v38, |v104|
	v_add_f32_e64 v39, v39, |v105|
	v_add_f32_e32 v38, v38, v39
	v_add_f32_e32 v24, v24, v38
	s_nop 1
	v_mfma_f32_32x32x16_f16 v[96:111], v[32:35], v[72:75], 0
	v_add_f32_e64 v38, |v112|, |v113|
	v_add_f32_e64 v39, |v114|, |v115|
	v_add_f32_e64 v38, v38, |v116|
	v_add_f32_e64 v39, v39, |v117|
	v_add_f32_e64 v38, v38, |v118|
	v_add_f32_e64 v39, v39, |v119|
	v_add_f32_e64 v38, v38, |v120|
	v_add_f32_e64 v39, v39, |v121|
	v_add_f32_e32 v38, v38, v39
	v_add_f32_e32 v25, v25, v38
	s_nop 1
	v_mfma_f32_32x32x16_f16 v[112:127], v[32:35], v[76:79], 0
	v_add_f32_e64 v38, |v96|, |v97|
	v_add_f32_e64 v39, |v98|, |v99|
	v_add_f32_e64 v38, v38, |v100|
	v_add_f32_e64 v39, v39, |v101|
	v_add_f32_e64 v38, v38, |v102|
	v_add_f32_e64 v39, v39, |v103|
	v_add_f32_e64 v38, v38, |v104|
	v_add_f32_e64 v39, v39, |v105|
	v_add_f32_e32 v38, v38, v39
	v_add_f32_e32 v26, v26, v38
	s_nop 1
	v_mfma_f32_32x32x16_f16 v[96:111], v[32:35], v[80:83], 0
	v_add_f32_e64 v38, |v112|, |v113|
	v_add_f32_e64 v39, |v114|, |v115|
	v_add_f32_e64 v38, v38, |v116|
	v_add_f32_e64 v39, v39, |v117|
	v_add_f32_e64 v38, v38, |v118|
	v_add_f32_e64 v39, v39, |v119|
	v_add_f32_e64 v38, v38, |v120|
	v_add_f32_e64 v39, v39, |v121|
	v_add_f32_e32 v38, v38, v39
	v_add_f32_e32 v27, v27, v38
	s_nop 1
	v_mfma_f32_32x32x16_f16 v[112:127], v[32:35], v[84:87], 0
	v_add_f32_e64 v38, |v96|, |v97|
	v_add_f32_e64 v39, |v98|, |v99|
	v_add_f32_e64 v38, v38, |v100|
	v_add_f32_e64 v39, v39, |v101|
	v_add_f32_e64 v38, v38, |v102|
	v_add_f32_e64 v39, v39, |v103|
	v_add_f32_e64 v38, v38, |v104|
	v_add_f32_e64 v39, v39, |v105|
	v_add_f32_e32 v38, v38, v39
	v_add_f32_e32 v28, v28, v38
	s_nop 1
	v_mfma_f32_32x32x16_f16 v[96:111], v[32:35], v[88:91], 0
	v_add_f32_e64 v38, |v112|, |v113|
	v_add_f32_e64 v39, |v114|, |v115|
	v_add_f32_e64 v38, v38, |v116|
	v_add_f32_e64 v39, v39, |v117|
	v_add_f32_e64 v38, v38, |v118|
	v_add_f32_e64 v39, v39, |v119|
	v_add_f32_e64 v38, v38, |v120|
	v_add_f32_e64 v39, v39, |v121|
	v_add_f32_e32 v38, v38, v39
	v_add_f32_e32 v29, v29, v38
	s_nop 1
	v_mfma_f32_32x32x16_f16 v[112:127], v[32:35], v[92:95], 0
	v_add_f32_e64 v38, |v96|, |v97|
	v_add_f32_e64 v39, |v98|, |v99|
	v_add_f32_e64 v38, v38, |v100|
	v_add_f32_e64 v39, v39, |v101|
	v_add_f32_e64 v38, v38, |v102|
	v_add_f32_e64 v39, v39, |v103|
	v_add_f32_e64 v38, v38, |v104|
	v_add_f32_e64 v39, v39, |v105|
	v_add_f32_e32 v38, v38, v39
	v_add_f32_e32 v30, v30, v38
	s_nop 1
	v_add_f32_e64 v38, |v112|, |v113|
	v_add_f32_e64 v39, |v114|, |v115|
	v_add_f32_e64 v38, v38, |v116|
	v_add_f32_e64 v39, v39, |v117|
	v_add_f32_e64 v38, v38, |v118|
	v_add_f32_e64 v39, v39, |v119|
	v_add_f32_e64 v38, v38, |v120|
	v_add_f32_e64 v39, v39, |v121|
	v_add_f32_e32 v38, v38, v39
	v_add_f32_e32 v31, v31, v38
	s_nop 1
	s_branch .Lsub_next
.Ln11:
	v_add_f32_e64 v38, |v96|, |v97|
	v_add_f32_e64 v39, |v98|, |v99|
	v_add_f32_e64 v38, v38, |v100|
	v_add_f32_e64 v39, v39, |v101|
	v_add_f32_e64 v38, v38, |v102|
	v_add_f32_e64 v39, v39, |v103|
	v_add_f32_e64 v38, v38, |v104|
	v_add_f32_e64 v39, v39, |v105|
	v_add_f32_e64 v38, v38, |v106|
	v_add_f32_e32 v38, v38, v39
	v_add_f32_e32 v24, v24, v38
	s_nop 0
	v_mfma_f32_32x32x16_f16 v[96:111], v[32:35], v[72:75], 0
	v_add_f32_e64 v38, |v112|, |v113|
	v_add_f32_e64 v39, |v114|, |v115|
	v_add_f32_e64 v38, v38, |v116|
	v_add_f32_e64 v39, v39, |v117|
	v_add_f32_e64 v38, v38, |v118|
	v_add_f32_e64 v39, v39, |v119|
	v_add_f32_e64 v38, v38, |v120|
	v_add_f32_e64 v39, v39, |v121|
	v_add_f32_e64 v38, v38, |v122|
	v_add_f32_e32 v38, v38, v39
	v_add_f32_e32 v25, v25, v38
	s_nop 0
	v_mfma_f32_32x32x16_f16 v[112:127], v[32:35], v[76:79], 0
	v_add_f32_e64 v38, |v96|, |v97|
	v_add_f32_e64 v39, |v98|, |v99|
	v_add_f32_e64 v38, v38, |v100|
	v_add_f32_e64 v39, v39, |v101|
	v_add_f32_e64 v38, v38, |v102|
	v_add_f32_e64 v39, v39, |v103|
	v_add_f32_e64 v38, v38, |v104|
	v_add_f32_e64 v39, v39, |v105|
	v_add_f32_e64 v38, v38, |v106|
	v_add_f32_e32 v38, v38, v39
	v_add_f32_e32 v26, v26, v38
	s_nop 0
	v_mfma_f32_32x32x16_f16 v[96:111], v[32:35], v[80:83], 0
	v_add_f32_e64 v38, |v112|, |v113|
	v_add_f32_e64 v39, |v114|, |v115|
	v_add_f32_e64 v38, v38, |v116|
	v_add_f32_e64 v39, v39, |v117|
	v_add_f32_e64 v38, v38, |v118|
	v_add_f32_e64 v39, v39, |v119|
	v_add_f32_e64 v38, v38, |v120|
	v_add_f32_e64 v39, v39, |v121|
	v_add_f32_e64 v38, v38, |v122|
	v_add_f32_e32 v38, v38, v39
	v_add_f32_e32 v27, v27, v38
	s_nop 0
	v_mfma_f32_32x32x16_f16 v[112:127], v[32:35], v[84:87], 0
	v_add_f32_e64 v38, |v96|, |v97|
	v_add_f32_e64 v39, |v98|, |v99|
	v_add_f32_e64 v38, v38, |v100|
	v_add_f32_e64 v39, v39, |v101|
	v_add_f32_e64 v38, v38, |v102|
	v_add_f32_e64 v39, v39, |v103|
	v_add_f32_e64 v38, v38, |v104|
	v_add_f32_e64 v39, v39, |v105|
	v_add_f32_e64 v38, v38, |v106|
	v_add_f32_e32 v38, v38, v39
	v_add_f32_e32 v28, v28, v38
	s_nop 0
	v_mfma_f32_32x32x16_f16 v[96:111], v[32:35], v[88:91], 0
	v_add_f32_e64 v38, |v112|, |v113|
	v_add_f32_e64 v39, |v114|, |v115|
	v_add_f32_e64 v38, v38, |v116|
	v_add_f32_e64 v39, v39, |v117|
	v_add_f32_e64 v38, v38, |v118|
	v_add_f32_e64 v39, v39, |v119|
	v_add_f32_e64 v38, v38, |v120|
	v_add_f32_e64 v39, v39, |v121|
	v_add_f32_e64 v38, v38, |v122|
	v_add_f32_e32 v38, v38, v39
	v_add_f32_e32 v29, v29, v38
	s_nop 0
	v_mfma_f32_32x32x16_f16 v[112:127], v[32:35], v[92:95], 0
	v_add_f32_e64 v38, |v96|, |v97|
	v_add_f32_e64 v39, |v98|, |v99|
	v_add_f32_e64 v38, v38, |v100|
	v_add_f32_e64 v39, v39, |v101|
	v_add_f32_e64 v38, v38, |v102|
	v_add_f32_e64 v39, v39, |v103|
	v_add_f32_e64 v38, v38, |v104|
	v_add_f32_e64 v39, v39, |v105|
	v_add_f32_e64 v38, v38, |v106|
	v_add_f32_e32 v38, v38, v39
	v_add_f32_e32 v30, v30, v38
	s_nop 0
	v_add_f32_e64 v38, |v112|, |v113|
	v_add_f32_e64 v39, |v114|, |v115|
	v_add_f32_e64 v38, v38, |v116|
	v_add_f32_e64 v39, v39, |v117|
	v_add_f32_e64 v38, v38, |v118|
	v_add_f32_e64 v39, v39, |v119|
	v_add_f32_e64 v38, v38, |v120|
	v_add_f32_e64 v39, v39, |v121|
	v_add_f32_e64 v38, v38, |v122|
	v_add_f32_e32 v38, v38, v39
	v_add_f32_e32 v31, v31, v38
	s_nop 0
	s_branch .Lsub_next

.Ln13:
	v_add_f32_e64 v38, |v96|, |v97|
	v_add_f32_e64 v39, |v98|, |v99|
	v_add_f32_e64 v38, v38, |v100|
	v_add_f32_e64 v39, v39, |v101|
	v_add_f32_e64 v38, v38, |v102|
	v_add_f32_e64 v39, v39, |v103|
	v_add_f32_e64 v38, v38, |v104|
	v_add_f32_e64 v39, v39, |v105|
	v_add_f32_e64 v38, v38, |v106|
	v_add_f32_e64 v39, v39, |v107|
	v_add_f32_e64 v38, v38, |v108|
	v_add_f32_e32 v38, v38, v39
	v_add_f32_e32 v24, v24, v38
	v_mfma_f32_32x32x16_f16 v[96:111], v[32:35], v[72:75], 0
	v_add_f32_e64 v38, |v112|, |v113|
	v_add_f32_e64 v39, |v114|, |v115|
	v_add_f32_e64 v38, v38, |v116|
	v_add_f32_e64 v39, v39, |v117|
	v_add_f32_e64 v38, v38, |v118|
	v_add_f32_e64 v39, v39, |v119|
	v_add_f32_e64 v38, v38, |v120|
	v_add_f32_e64 v39, v39, |v121|
	v_add_f32_e64 v38, v38, |v122|
	v_add_f32_e64 v39, v39, |v123|
	v_add_f32_e64 v38, v38, |v124|
	v_add_f32_e32 v38, v38, v39
	v_add_f32_e32 v25, v25, v38
	v_mfma_f32_32x32x16_f16 v[112:127], v[32:35], v[76:79], 0
	v_add_f32_e64 v38, |v96|, |v97|
	v_add_f32_e64 v39, |v98|, |v99|
	v_add_f32_e64 v38, v38, |v100|
	v_add_f32_e64 v39, v39, |v101|
	v_add_f32_e64 v38, v38, |v102|
	v_add_f32_e64 v39, v39, |v103|
	v_add_f32_e64 v38, v38, |v104|
	v_add_f32_e64 v39, v39, |v105|
	v_add_f32_e64 v38, v38, |v106|
	v_add_f32_e64 v39, v39, |v107|
	v_add_f32_e64 v38, v38, |v108|
	v_add_f32_e32 v38, v38, v39
	v_add_f32_e32 v26, v26, v38
	v_mfma_f32_32x32x16_f16 v[96:111], v[32:35], v[80:83], 0
	v_add_f32_e64 v38, |v112|, |v113|
	v_add_f32_e64 v39, |v114|, |v115|
	v_add_f32_e64 v38, v38, |v116|
	v_add_f32_e64 v39, v39, |v117|
	v_add_f32_e64 v38, v38, |v118|
	v_add_f32_e64 v39, v39, |v119|
	v_add_f32_e64 v38, v38, |v120|
	v_add_f32_e64 v39, v39, |v121|
	v_add_f32_e64 v38, v38, |v122|
	v_add_f32_e64 v39, v39, |v123|
	v_add_f32_e64 v38, v38, |v124|
	v_add_f32_e32 v38, v38, v39
	v_add_f32_e32 v27, v27, v38
	v_mfma_f32_32x32x16_f16 v[112:127], v[32:35], v[84:87], 0
	v_add_f32_e64 v38, |v96|, |v97|
	v_add_f32_e64 v39, |v98|, |v99|
	v_add_f32_e64 v38, v38, |v100|
	v_add_f32_e64 v39, v39, |v101|
	v_add_f32_e64 v38, v38, |v102|
	v_add_f32_e64 v39, v39, |v103|
	v_add_f32_e64 v38, v38, |v104|
	v_add_f32_e64 v39, v39, |v105|
	v_add_f32_e64 v38, v38, |v106|
	v_add_f32_e64 v39, v39, |v107|
	v_add_f32_e64 v38, v38, |v108|
	v_add_f32_e32 v38, v38, v39
	v_add_f32_e32 v28, v28, v38
	v_mfma_f32_32x32x16_f16 v[96:111], v[32:35], v[88:91], 0
	v_add_f32_e64 v38, |v112|, |v113|
	v_add_f32_e64 v39, |v114|, |v115|
	v_add_f32_e64 v38, v38, |v116|
	v_add_f32_e64 v39, v39, |v117|
	v_add_f32_e64 v38, v38, |v118|
	v_add_f32_e64 v39, v39, |v119|
	v_add_f32_e64 v38, v38, |v120|
	v_add_f32_e64 v39, v39, |v121|
	v_add_f32_e64 v38, v38, |v122|
	v_add_f32_e64 v39, v39, |v123|
	v_add_f32_e64 v38, v38, |v124|
	v_add_f32_e32 v38, v38, v39
	v_add_f32_e32 v29, v29, v38
	v_mfma_f32_32x32x16_f16 v[112:127], v[32:35], v[92:95], 0
	v_add_f32_e64 v38, |v96|, |v97|
	v_add_f32_e64 v39, |v98|, |v99|
	v_add_f32_e64 v38, v38, |v100|
	v_add_f32_e64 v39, v39, |v101|
	v_add_f32_e64 v38, v38, |v102|
	v_add_f32_e64 v39, v39, |v103|
	v_add_f32_e64 v38, v38, |v104|
	v_add_f32_e64 v39, v39, |v105|
	v_add_f32_e64 v38, v38, |v106|
	v_add_f32_e64 v39, v39, |v107|
	v_add_f32_e64 v38, v38, |v108|
	v_add_f32_e32 v38, v38, v39
	v_add_f32_e32 v30, v30, v38
	v_add_f32_e64 v38, |v112|, |v113|
	v_add_f32_e64 v39, |v114|, |v115|
	v_add_f32_e64 v38, v38, |v116|
	v_add_f32_e64 v39, v39, |v117|
	v_add_f32_e64 v38, v38, |v118|
	v_add_f32_e64 v39, v39, |v119|
	v_add_f32_e64 v38, v38, |v120|
	v_add_f32_e64 v39, v39, |v121|
	v_add_f32_e64 v38, v38, |v122|
	v_add_f32_e64 v39, v39, |v123|
	v_add_f32_e64 v38, v38, |v124|
	v_add_f32_e32 v38, v38, v39
	v_add_f32_e32 v31, v31, v38
	s_branch .Lsub_next
.Ln14:
	v_add_f32_e64 v38, |v96|, |v97|
	v_add_f32_e64 v39, |v98|, |v99|
	v_add_f32_e64 v38, v38, |v100|
	v_add_f32_e64 v39, v39, |v101|
	v_add_f32_e64 v38, v38, |v102|
	v_add_f32_e64 v39, v39, |v103|
	v_add_f32_e64 v38, v38, |v104|
	v_add_f32_e64 v39, v39, |v105|
	v_add_f32_e64 v38, v38, |v106|
	v_add_f32_e64 v39, v39, |v107|
	v_add_f32_e64 v38, v38, |v108|
	v_add_f32_e64 v39, v39, |v109|
	v_add_f32_e32 v38, v38, v39
	v_add_f32_e32 v24, v24, v38
	v_mfma_f32_32x32x16_f16 v[96:111], v[32:35], v[72:75], 0
	v_add_f32_e64 v38, |v112|, |v113|
	v_add_f32_e64 v39, |v114|, |v115|
	v_add_f32_e64 v38, v38, |v116|
	v_add_f32_e64 v39, v39, |v117|
	v_add_f32_e64 v38, v38, |v118|
	v_add_f32_e64 v39, v39, |v119|
	v_add_f32_e64 v38, v38, |v120|
	v_add_f32_e64 v39, v39, |v121|
	v_add_f32_e64 v38, v38, |v122|
	v_add_f32_e64 v39, v39, |v123|
	v_add_f32_e64 v38, v38, |v124|
	v_add_f32_e64 v39, v39, |v125|
	v_add_f32_e32 v38, v38, v39
	v_add_f32_e32 v25, v25, v38
	v_mfma_f32_32x32x16_f16 v[112:127], v[32:35], v[76:79], 0
	v_add_f32_e64 v38, |v96|, |v97|
	v_add_f32_e64 v39, |v98|, |v99|
	v_add_f32_e64 v38, v38, |v100|
	v_add_f32_e64 v39, v39, |v101|
	v_add_f32_e64 v38, v38, |v102|
	v_add_f32_e64 v39, v39, |v103|
	v_add_f32_e64 v38, v38, |v104|
	v_add_f32_e64 v39, v39, |v105|
	v_add_f32_e64 v38, v38, |v106|
	v_add_f32_e64 v39, v39, |v107|
	v_add_f32_e64 v38, v38, |v108|
	v_add_f32_e64 v39, v39, |v109|
	v_add_f32_e32 v38, v38, v39
	v_add_f32_e32 v26, v26, v38
	v_mfma_f32_32x32x16_f16 v[96:111], v[32:35], v[80:83], 0
	v_add_f32_e64 v38, |v112|, |v113|
	v_add_f32_e64 v39, |v114|, |v115|
	v_add_f32_e64 v38, v38, |v116|
	v_add_f32_e64 v39, v39, |v117|
	v_add_f32_e64 v38, v38, |v118|
	v_add_f32_e64 v39, v39, |v119|
	v_add_f32_e64 v38, v38, |v120|
	v_add_f32_e64 v39, v39, |v121|
	v_add_f32_e64 v38, v38, |v122|
	v_add_f32_e64 v39, v39, |v123|
	v_add_f32_e64 v38, v38, |v124|
	v_add_f32_e64 v39, v39, |v125|
	v_add_f32_e32 v38, v38, v39
	v_add_f32_e32 v27, v27, v38
	v_mfma_f32_32x32x16_f16 v[112:127], v[32:35], v[84:87], 0
	v_add_f32_e64 v38, |v96|, |v97|
	v_add_f32_e64 v39, |v98|, |v99|
	v_add_f32_e64 v38, v38, |v100|
	v_add_f32_e64 v39, v39, |v101|
	v_add_f32_e64 v38, v38, |v102|
	v_add_f32_e64 v39, v39, |v103|
	v_add_f32_e64 v38, v38, |v104|
	v_add_f32_e64 v39, v39, |v105|
	v_add_f32_e64 v38, v38, |v106|
	v_add_f32_e64 v39, v39, |v107|
	v_add_f32_e64 v38, v38, |v108|
	v_add_f32_e64 v39, v39, |v109|
	v_add_f32_e32 v38, v38, v39
	v_add_f32_e32 v28, v28, v38
	v_mfma_f32_32x32x16_f16 v[96:111], v[32:35], v[88:91], 0
	v_add_f32_e64 v38, |v112|, |v113|
	v_add_f32_e64 v39, |v114|, |v115|
	v_add_f32_e64 v38, v38, |v116|
	v_add_f32_e64 v39, v39, |v117|
	v_add_f32_e64 v38, v38, |v118|
	v_add_f32_e64 v39, v39, |v119|
	v_add_f32_e64 v38, v38, |v120|
	v_add_f32_e64 v39, v39, |v121|
	v_add_f32_e64 v38, v38, |v122|
	v_add_f32_e64 v39, v39, |v123|
	v_add_f32_e64 v38, v38, |v124|
	v_add_f32_e64 v39, v39, |v125|
	v_add_f32_e32 v38, v38, v39
	v_add_f32_e32 v29, v29, v38
	v_mfma_f32_32x32x16_f16 v[112:127], v[32:35], v[92:95], 0
	v_add_f32_e64 v38, |v96|, |v97|
	v_add_f32_e64 v39, |v98|, |v99|
	v_add_f32_e64 v38, v38, |v100|
	v_add_f32_e64 v39, v39, |v101|
	v_add_f32_e64 v38, v38, |v102|
	v_add_f32_e64 v39, v39, |v103|
	v_add_f32_e64 v38, v38, |v104|
	v_add_f32_e64 v39, v39, |v105|
	v_add_f32_e64 v38, v38, |v106|
	v_add_f32_e64 v39, v39, |v107|
	v_add_f32_e64 v38, v38, |v108|
	v_add_f32_e64 v39, v39, |v109|
	v_add_f32_e32 v38, v38, v39
	v_add_f32_e32 v30, v30, v38
	v_add_f32_e64 v38, |v112|, |v113|
	v_add_f32_e64 v39, |v114|, |v115|
	v_add_f32_e64 v38, v38, |v116|
	v_add_f32_e64 v39, v39, |v117|
	v_add_f32_e64 v38, v38, |v118|
	v_add_f32_e64 v39, v39, |v119|
	v_add_f32_e64 v38, v38, |v120|
	v_add_f32_e64 v39, v39, |v121|
	v_add_f32_e64 v38, v38, |v122|
	v_add_f32_e64 v39, v39, |v123|
	v_add_f32_e64 v38, v38, |v124|
	v_add_f32_e64 v39, v39, |v125|
	v_add_f32_e32 v38, v38, v39
	v_add_f32_e32 v31, v31, v38
	s_branch .Lsub_next
.Ln15:
	v_add_f32_e64 v38, |v96|, |v97|
	v_add_f32_e64 v39, |v98|, |v99|
	v_add_f32_e64 v38, v38, |v100|
	v_add_f32_e64 v39, v39, |v101|
	v_add_f32_e64 v38, v38, |v102|
	v_add_f32_e64 v39, v39, |v103|
	v_add_f32_e64 v38, v38, |v104|
	v_add_f32_e64 v39, v39, |v105|
	v_add_f32_e64 v38, v38, |v106|
	v_add_f32_e64 v39, v39, |v107|
	v_add_f32_e64 v38, v38, |v108|
	v_add_f32_e64 v39, v39, |v109|
	v_add_f32_e64 v38, v38, |v110|
	v_add_f32_e32 v38, v38, v39
	v_add_f32_e32 v24, v24, v38
	v_mfma_f32_32x32x16_f16 v[96:111], v[32:35], v[72:75], 0
	v_add_f32_e64 v38, |v112|, |v113|
	v_add_f32_e64 v39, |v114|, |v115|
	v_add_f32_e64 v38, v38, |v116|
	v_add_f32_e64 v39, v39, |v117|
	v_add_f32_e64 v38, v38, |v118|
	v_add_f32_e64 v39, v39, |v119|
	v_add_f32_e64 v38, v38, |v120|
	v_add_f32_e64 v39, v39, |v121|
	v_add_f32_e64 v38, v38, |v122|
	v_add_f32_e64 v39, v39, |v123|
	v_add_f32_e64 v38, v38, |v124|
	v_add_f32_e64 v39, v39, |v125|
	v_add_f32_e64 v38, v38, |v126|
	v_add_f32_e32 v38, v38, v39
	v_add_f32_e32 v25, v25, v38
	v_mfma_f32_32x32x16_f16 v[112:127], v[32:35], v[76:79], 0
	v_add_f32_e64 v38, |v96|, |v97|
	v_add_f32_e64 v39, |v98|, |v99|
	v_add_f32_e64 v38, v38, |v100|
	v_add_f32_e64 v39, v39, |v101|
	v_add_f32_e64 v38, v38, |v102|
	v_add_f32_e64 v39, v39, |v103|
	v_add_f32_e64 v38, v38, |v104|
	v_add_f32_e64 v39, v39, |v105|
	v_add_f32_e64 v38, v38, |v106|
	v_add_f32_e64 v39, v39, |v107|
	v_add_f32_e64 v38, v38, |v108|
	v_add_f32_e64 v39, v39, |v109|
	v_add_f32_e64 v38, v38, |v110|
	v_add_f32_e32 v38, v38, v39
	v_add_f32_e32 v26, v26, v38
	v_mfma_f32_32x32x16_f16 v[96:111], v[32:35], v[80:83], 0
	v_add_f32_e64 v38, |v112|, |v113|
	v_add_f32_e64 v39, |v114|, |v115|
	v_add_f32_e64 v38, v38, |v116|
	v_add_f32_e64 v39, v39, |v117|
	v_add_f32_e64 v38, v38, |v118|
	v_add_f32_e64 v39, v39, |v119|
	v_add_f32_e64 v38, v38, |v120|
	v_add_f32_e64 v39, v39, |v121|
	v_add_f32_e64 v38, v38, |v122|
	v_add_f32_e64 v39, v39, |v123|
	v_add_f32_e64 v38, v38, |v124|
	v_add_f32_e64 v39, v39, |v125|
	v_add_f32_e64 v38, v38, |v126|
	v_add_f32_e32 v38, v38, v39
	v_add_f32_e32 v27, v27, v38
	v_mfma_f32_32x32x16_f16 v[112:127], v[32:35], v[84:87], 0
	v_add_f32_e64 v38, |v96|, |v97|
	v_add_f32_e64 v39, |v98|, |v99|
	v_add_f32_e64 v38, v38, |v100|
	v_add_f32_e64 v39, v39, |v101|
	v_add_f32_e64 v38, v38, |v102|
	v_add_f32_e64 v39, v39, |v103|
	v_add_f32_e64 v38, v38, |v104|
	v_add_f32_e64 v39, v39, |v105|
	v_add_f32_e64 v38, v38, |v106|
	v_add_f32_e64 v39, v39, |v107|
	v_add_f32_e64 v38, v38, |v108|
	v_add_f32_e64 v39, v39, |v109|
	v_add_f32_e64 v38, v38, |v110|
	v_add_f32_e32 v38, v38, v39
	v_add_f32_e32 v28, v28, v38
	v_mfma_f32_32x32x16_f16 v[96:111], v[32:35], v[88:91], 0
	v_add_f32_e64 v38, |v112|, |v113|
	v_add_f32_e64 v39, |v114|, |v115|
	v_add_f32_e64 v38, v38, |v116|
	v_add_f32_e64 v39, v39, |v117|
	v_add_f32_e64 v38, v38, |v118|
	v_add_f32_e64 v39, v39, |v119|
	v_add_f32_e64 v38, v38, |v120|
	v_add_f32_e64 v39, v39, |v121|
	v_add_f32_e64 v38, v38, |v122|
	v_add_f32_e64 v39, v39, |v123|
	v_add_f32_e64 v38, v38, |v124|
	v_add_f32_e64 v39, v39, |v125|
	v_add_f32_e64 v38, v38, |v126|
	v_add_f32_e32 v38, v38, v39
	v_add_f32_e32 v29, v29, v38
	v_mfma_f32_32x32x16_f16 v[112:127], v[32:35], v[92:95], 0
	v_add_f32_e64 v38, |v96|, |v97|
	v_add_f32_e64 v39, |v98|, |v99|
	v_add_f32_e64 v38, v38, |v100|
	v_add_f32_e64 v39, v39, |v101|
	v_add_f32_e64 v38, v38, |v102|
	v_add_f32_e64 v39, v39, |v103|
	v_add_f32_e64 v38, v38, |v104|
	v_add_f32_e64 v39, v39, |v105|
	v_add_f32_e64 v38, v38, |v106|
	v_add_f32_e64 v39, v39, |v107|
	v_add_f32_e64 v38, v38, |v108|
	v_add_f32_e64 v39, v39, |v109|
	v_add_f32_e64 v38, v38, |v110|
	v_add_f32_e32 v38, v38, v39
	v_add_f32_e32 v30, v30, v38
	v_add_f32_e64 v38, |v112|, |v113|
	v_add_f32_e64 v39, |v114|, |v115|
	v_add_f32_e64 v38, v38, |v116|
	v_add_f32_e64 v39, v39, |v117|
	v_add_f32_e64 v38, v38, |v118|
	v_add_f32_e64 v39, v39, |v119|
	v_add_f32_e64 v38, v38, |v120|
	v_add_f32_e64 v39, v39, |v121|
	v_add_f32_e64 v38, v38, |v122|
	v_add_f32_e64 v39, v39, |v123|
	v_add_f32_e64 v38, v38, |v124|
	v_add_f32_e64 v39, v39, |v125|
	v_add_f32_e64 v38, v38, |v126|
	v_add_f32_e32 v38, v38, v39
	v_add_f32_e32 v31, v31, v38
	s_branch .Lsub_next
